# MLA: side-job tick moved behind the stage barrier (one combined non-MFMA section per stage instead of two); tick temporaries renamed to v164-v171/v178
# baseline (speedup 1.0000x reference)
; DEV void sj_tick(const Params& p, int layer, SideJob& sj, LAS char* lds, int tid) {
;     ...
;     if (ph == 0) {
;         const int krow = tid >> 4, c4 = (tid & 15) * 4;
;         const float* a0 = (d.mode == 0 || d.mode == 2) ? d.s0 + (size_t)(d.k0 + krow) * d.ld + d.nt * 64 + c4
;                                         : ((c4 < 32) ? d.s0 + (size_t)(d.k0 + krow) * 512 + d.nt * 32 + c4 : d.s1 + (size_t)(d.k0 + krow) * 512 + d.nt * 32 + c4 - 32);
;         sj.v0 = *(const f32x4*)a0; sj.v1 = *(const f32x4*)(a0 + (size_t)32 * d.ld);
.LBB0_810:
	s_lshl_b32 s30, s20, 7
	v_lshl_add_u64 v[164:165], v[166:167], 0, s[30:31]
	global_load_dwordx4 v[182:185], v[166:167], off
	global_load_dwordx4 v[186:189], v[164:165], off
	s_mov_b32 s21, s36
	s_mov_b32 s57, s33

; #define LAS __attribute__((address_space(3)))
; DEV float ex2(float x) { return __builtin_amdgcn_exp2f(x); }
; #define MLA_SB() __builtin_amdgcn_sched_barrier(0)
; #define MLA_PIN(x) asm volatile("" : "+v"(x))
; template <int VAR> DEV void mla_step(f32x16& C0, f32x16& C1, f32x16& P0, f32x16& P1, f32x16& o0, f32x16& o1, f32x16& lacc,
;                   const v8i (&qf)[2], const f32x16& cini, LAS char* kp, LAS char* vp, v8i& pw) {
;     v8i kf[2], vf[2];
;     const v8i ones8 = {0x38383838, 0x38383838, 0x38383838, 0x38383838, 0x38383838, 0x38383838, 0x38383838, 0x38383838};
;     kf[0] = mla_kf8(kp, 0, 0); kf[1] = mla_kf8(kp, 1, 0);
;     MLA_SB();
; #pragma unroll
;     for (int g = 0; g < 4; ++g) {
;         const int kb = g & 1, sx = g >> 1;
;         if (kb) C1 = MFMA8(kf[1], qf[sx], sx == 0 ? cini : C1); else C0 = MFMA8(kf[0], qf[sx], sx == 0 ? cini : C0);
;         if (g < 2) kf[kb] = mla_kf8(kp, kb, 1);
;         if (g >= 2) vf[g - 2] = mla_vf8(vp, g - 2);
; #pragma unroll
;         for (int j = 0; j < 2; ++j) { const int w = 2 * g + j, e = 4 * w;
;             if (VAR == 3) pw[w] = __builtin_bit_cast(int, (e < 16) ? P0[e] : P1[e - 16]);
;             else pw[w] = (int)((e < 16) ? pk_bf8x4(P0[e], P0[e + 1], P0[e + 2], P0[e + 3], pw[w]) : pk_bf8x4(P1[e - 16], P1[e - 15], P1[e - 14], P1[e - 13], pw[w])); }
;         if (g == 3) MLA_PIN(pw);
;         MLA_SB();
;     }
; #pragma unroll
;     for (int g = 0; g < 3; ++g) {
;         if (g == 0) o0 = MFMA8PV(vf[0], pw, o0); else if (g == 1) o1 = MFMA8PV(vf[1], pw, o1); else lacc = MFMA8PV(ones8, pw, lacc);
;         const int e0 = (g * 32) / 3, e1 = ((g + 1) * 32) / 3;
; #pragma unroll
;         for (int e = e0; e < e1; ++e) { if (VAR == 2 || VAR == 3) continue; if (e < 16) C0[e] = ex2(C0[e]); else C1[e - 16] = ex2(C1[e - 16]); }
;         if (g < 2) MLA_PIN(C0);
;         if (g > 0) MLA_PIN(C1);
;         MLA_SB();
;     }
; }
; template <int VAR> DEV void mla_unit(const Params& p, int layer, int b, int hd, int tokbase, int t0, int t1, LAS char* lds, SideJob& sj) {
;     ...
;             if (s + 2 < ns) MLA_ISSUE(t0 + s + 2, (nslot == 2) ? 0 : nslot + 1);
;             { LAS char* nb = lds + nslot * STG; LAS char* ob = lds + slot * STG; mla_step<VAR>(sA0, sA1, sB0, sB1, o0, o1, lacc, qf, cini, nb + koffl, ob + MLA_VSUB + voffl, pw); }
.LBB0_812:
	s_mul_i32 s64, s62, 0x6000
	s_add_i32 s2, s64, 0x6000
	s_cmp_eq_u32 s62, 2
	s_cselect_b32 s2, 0, s2
	s_add_i32 s2, s2, s60
	s_mov_b32 s3, m0
	s_mov_b32 m0, s2
	v_add_u32_e32 v173, s64, v200
	ds_read_b128 v[66:69], v173
	ds_read_b128 v[74:77], v173 offset:512
	ds_read_b128 v[70:73], v173 offset:1024
	ds_read_b128 v[78:81], v173 offset:1536
	v_cvt_pk_bf8_f32 v146, v114, v115
	v_cvt_pk_bf8_f32 v147, v118, v119
	v_exp_f32_e32 v101, v101
	v_exp_f32_e32 v102, v102
	v_exp_f32_e32 v103, v103
	s_waitcnt lgkmcnt(1)
	v_mfma_scale_f32_32x32x64_f8f6f4 v[82:97], v[66:73], v[138:145], v[2:17], v209, v208 op_sel_hi:[0,0,0]
	global_load_lds_dwordx4 v[162:163], off
	ds_read_b128 v[164:167], v173 offset:4096
	ds_read_b128 v[168:171], v173 offset:5120
	v_cvt_pk_bf8_f32 v146, v116, v117 op_sel:[0,0,1]
	v_cvt_pk_bf8_f32 v147, v120, v121 op_sel:[0,0,1]
	v_cvt_pk_bf8_f32 v148, v122, v123
	v_cvt_pk_bf8_f32 v149, v126, v127
	ds_read_b128 v[114:117], v173 offset:4608
	ds_read_b128 v[118:121], v173 offset:5632
	v_exp_f32_e32 v104, v104
	v_exp_f32_e32 v105, v105
	s_waitcnt lgkmcnt(4)
	v_mfma_scale_f32_32x32x64_f8f6f4 v[66:81], v[74:81], v[138:145], v[2:17], v209, v208 op_sel_hi:[0,0,0]
	global_load_lds_dwordx4 v[162:163], off offset:1024
	v_cvt_pk_bf8_f32 v148, v124, v125 op_sel:[0,0,1]
	v_cvt_pk_bf8_f32 v149, v128, v129 op_sel:[0,0,1]
	ds_read_b128 v[122:125], v172 offset:20480
	ds_read_b128 v[126:129], v172 offset:21504
	v_exp_f32_e32 v106, v106
	v_exp_f32_e32 v107, v107
	v_exp_f32_e32 v108, v108
	s_waitcnt lgkmcnt(4)
	v_mfma_scale_f32_32x32x64_f8f6f4 v[82:97], v[164:171], v[130:137], v[82:97], v209, v208 op_sel_hi:[0,0,0]
	global_load_lds_dwordx4 v[162:163], off offset:2048
	s_mov_b32 m0, s3
	v_exp_f32_e32 v109, v109
	v_exp_f32_e32 v110, v110
	v_exp_f32_e32 v111, v111
	v_exp_f32_e32 v112, v112
	v_exp_f32_e32 v113, v113
	s_waitcnt lgkmcnt(2)
	v_mfma_scale_f32_32x32x64_f8f6f4 v[66:81], v[114:121], v[130:137], v[66:81], v209, v208 op_sel_hi:[0,0,0]
	v_cvt_pk_bf8_f32 v150, v98, v99
	v_cvt_pk_bf8_f32 v151, v102, v103
	v_cvt_pk_bf8_f32 v150, v100, v101 op_sel:[0,0,1]
	v_cvt_pk_bf8_f32 v151, v104, v105 op_sel:[0,0,1]
	v_cvt_pk_bf8_f32 v152, v106, v107
	v_cvt_pk_bf8_f32 v153, v110, v111
	v_cvt_pk_bf8_f32 v152, v108, v109 op_sel:[0,0,1]
	v_cvt_pk_bf8_f32 v153, v112, v113 op_sel:[0,0,1]
	ds_read_b128 v[98:101], v172 offset:20992
	ds_read_b128 v[102:105], v172 offset:22016
	s_waitcnt lgkmcnt(2)
	v_mfma_scale_f32_32x32x64_f8f6f4 v[50:65], v[122:129], v[146:153], v[50:65], v209, v209 op_sel_hi:[0,0,0] blgp:1
	s_nop 0
	v_exp_f32_e32 v82, v82
	v_exp_f32_e32 v83, v83
	v_exp_f32_e32 v84, v84
	v_exp_f32_e32 v85, v85
	v_exp_f32_e32 v86, v86
	v_exp_f32_e32 v87, v87
	s_waitcnt lgkmcnt(0)
	v_mfma_scale_f32_32x32x64_f8f6f4 v[18:33], v[98:105], v[146:153], v[18:33], v209, v209 op_sel_hi:[0,0,0] blgp:1
	v_exp_f32_e32 v88, v88
	v_exp_f32_e32 v89, v89
	v_exp_f32_e32 v90, v90
	v_exp_f32_e32 v91, v91
	v_exp_f32_e32 v92, v92
	v_exp_f32_e32 v93, v93
	v_mfma_scale_f32_32x32x64_f8f6f4 v[34:49], v[210:217], v[146:153], v[34:49], v209, v209 op_sel_hi:[0,0,0] blgp:1
	v_exp_f32_e32 v94, v94
	v_exp_f32_e32 v95, v95
	v_exp_f32_e32 v96, v96
	v_exp_f32_e32 v97, v97
	v_exp_f32_e32 v66, v66
	v_exp_f32_e32 v67, v67
	v_exp_f32_e32 v68, v68
	s_mov_b64 s[20:21], 0x6000
	s_cmpk_lg_i32 s61, 0x80
	v_lshl_add_u64 v[162:163], v[162:163], 0, s[20:21]
	s_cbranch_scc0 .LBB0_835
; #define LAS __attribute__((address_space(3)))
; #define WAITV(n) asm volatile("s_waitcnt vmcnt(%0)" ::"n"(n) : "memory")
; DEV float ex2(float x) { return __builtin_amdgcn_exp2f(x); }
; #define MLA_SB() __builtin_amdgcn_sched_barrier(0)
; template <int VAR> DEV void mla_step(f32x16& C0, f32x16& C1, f32x16& P0, f32x16& P1, f32x16& o0, f32x16& o1, f32x16& lacc,
;                   const v8i (&qf)[2], const f32x16& cini, LAS char* kp, LAS char* vp, v8i& pw) {
;     v8i kf[2], vf[2];
;     const v8i ones8 = {0x38383838, 0x38383838, 0x38383838, 0x38383838, 0x38383838, 0x38383838, 0x38383838, 0x38383838};
;     kf[0] = mla_kf8(kp, 0, 0); kf[1] = mla_kf8(kp, 1, 0);
;     MLA_SB();
; #pragma unroll
;     for (int g = 0; g < 4; ++g) {
;         const int kb = g & 1, sx = g >> 1;
;         if (kb) C1 = MFMA8(kf[1], qf[sx], sx == 0 ? cini : C1); else C0 = MFMA8(kf[0], qf[sx], sx == 0 ? cini : C0);
;         if (g < 2) kf[kb] = mla_kf8(kp, kb, 1);
;         if (g >= 2) vf[g - 2] = mla_vf8(vp, g - 2);
; #pragma unroll
;         for (int j = 0; j < 2; ++j) { const int w = 2 * g + j, e = 4 * w;
;             if (VAR == 3) pw[w] = __builtin_bit_cast(int, (e < 16) ? P0[e] : P1[e - 16]);
;             else pw[w] = (int)((e < 16) ? pk_bf8x4(P0[e], P0[e + 1], P0[e + 2], P0[e + 3], pw[w]) : pk_bf8x4(P1[e - 16], P1[e - 15], P1[e - 14], P1[e - 13], pw[w])); }
;         if (g == 3) MLA_PIN(pw);
;         MLA_SB();
;     }
; #pragma unroll
;     for (int g = 0; g < 3; ++g) {
;         if (g == 0) o0 = MFMA8PV(vf[0], pw, o0); else if (g == 1) o1 = MFMA8PV(vf[1], pw, o1); else lacc = MFMA8PV(ones8, pw, lacc);
;         const int e0 = (g * 32) / 3, e1 = ((g + 1) * 32) / 3;
; #pragma unroll
;         for (int e = e0; e < e1; ++e) { if (VAR == 2 || VAR == 3) continue; if (e < 16) C0[e] = ex2(C0[e]); else C1[e - 16] = ex2(C1[e - 16]); }
;         if (g < 2) MLA_PIN(C0);
;         if (g > 0) MLA_PIN(C1);
;         MLA_SB();
;     }
; }
; template <int VAR> DEV void mla_unit(const Params& p, int layer, int b, int hd, int tokbase, int t0, int t1, LAS char* lds, SideJob& sj) {
;     ...
;         sj_tick(p, layer, sj, lds, tid);
;         { LAS char* base = lds + slot * STG; mla_step<VAR>(sB0, sB1, sA0, sA1, o0, o1, lacc, qf, cini, base + MLA_KSUB + koffl, base + voffl, pw); }
;         if (s + 1 < ns) {
;             const int nslot = (slot == 2) ? 0 : slot + 1;
;             WAITV(0); SBAR();
.LBB0_813:
	s_mul_i32 s2, s62, 0x6000
	v_add_u32_e32 v172, s2, v200
	ds_read_b128 v[98:101], v172 offset:8192
	ds_read_b128 v[106:109], v172 offset:8704
	ds_read_b128 v[102:105], v172 offset:9216
	ds_read_b128 v[110:113], v172 offset:9728
	v_cvt_pk_bf8_f32 v146, v82, v83
	v_cvt_pk_bf8_f32 v147, v86, v87
	v_exp_f32_e32 v69, v69
	v_exp_f32_e32 v70, v70
	v_exp_f32_e32 v71, v71
	s_waitcnt lgkmcnt(1)
	v_mfma_scale_f32_32x32x64_f8f6f4 v[114:129], v[98:105], v[138:145], v[2:17], v209, v208 op_sel_hi:[0,0,0]
	ds_read_b128 v[154:157], v172 offset:12288
	ds_read_b128 v[158:161], v172 offset:13312
	v_cvt_pk_bf8_f32 v146, v84, v85 op_sel:[0,0,1]
	v_cvt_pk_bf8_f32 v147, v88, v89 op_sel:[0,0,1]
	v_cvt_pk_bf8_f32 v148, v90, v91
	v_cvt_pk_bf8_f32 v149, v94, v95
	ds_read_b128 v[82:85], v172 offset:12800
	ds_read_b128 v[86:89], v172 offset:13824
	v_exp_f32_e32 v72, v72
	v_exp_f32_e32 v73, v73
	s_waitcnt lgkmcnt(4)
	v_mfma_scale_f32_32x32x64_f8f6f4 v[98:113], v[106:113], v[138:145], v[2:17], v209, v208 op_sel_hi:[0,0,0]
	v_cvt_pk_bf8_f32 v148, v92, v93 op_sel:[0,0,1]
	v_cvt_pk_bf8_f32 v149, v96, v97 op_sel:[0,0,1]
	ds_read_b128 v[90:93], v172 offset:16384
	ds_read_b128 v[94:97], v172 offset:17408
	v_exp_f32_e32 v74, v74
	v_exp_f32_e32 v75, v75
	v_exp_f32_e32 v76, v76
	s_waitcnt lgkmcnt(4)
	v_mfma_scale_f32_32x32x64_f8f6f4 v[114:129], v[154:161], v[130:137], v[114:129], v209, v208 op_sel_hi:[0,0,0]
	v_exp_f32_e32 v77, v77
	v_exp_f32_e32 v78, v78
	v_exp_f32_e32 v79, v79
	v_exp_f32_e32 v80, v80
	v_exp_f32_e32 v81, v81
	s_waitcnt lgkmcnt(2)
	v_mfma_scale_f32_32x32x64_f8f6f4 v[98:113], v[82:89], v[130:137], v[98:113], v209, v208 op_sel_hi:[0,0,0]
	v_cvt_pk_bf8_f32 v150, v66, v67
	v_cvt_pk_bf8_f32 v151, v70, v71
	v_cvt_pk_bf8_f32 v150, v68, v69 op_sel:[0,0,1]
	v_cvt_pk_bf8_f32 v151, v72, v73 op_sel:[0,0,1]
	v_cvt_pk_bf8_f32 v152, v74, v75
	v_cvt_pk_bf8_f32 v153, v78, v79
	v_cvt_pk_bf8_f32 v152, v76, v77 op_sel:[0,0,1]
	v_cvt_pk_bf8_f32 v153, v80, v81 op_sel:[0,0,1]
	ds_read_b128 v[66:69], v172 offset:16896
	ds_read_b128 v[70:73], v172 offset:17920
	s_waitcnt lgkmcnt(2)
	v_mfma_scale_f32_32x32x64_f8f6f4 v[50:65], v[90:97], v[146:153], v[50:65], v209, v209 op_sel_hi:[0,0,0] blgp:1
	s_nop 0
	v_exp_f32_e32 v114, v114
	v_exp_f32_e32 v115, v115
	v_exp_f32_e32 v116, v116
	v_exp_f32_e32 v117, v117
	v_exp_f32_e32 v118, v118
	v_exp_f32_e32 v119, v119
	s_waitcnt lgkmcnt(0)
	v_mfma_scale_f32_32x32x64_f8f6f4 v[18:33], v[66:73], v[146:153], v[18:33], v209, v209 op_sel_hi:[0,0,0] blgp:1
	v_exp_f32_e32 v120, v120
	v_exp_f32_e32 v121, v121
	v_exp_f32_e32 v122, v122
	v_exp_f32_e32 v123, v123
	v_exp_f32_e32 v124, v124
	v_exp_f32_e32 v125, v125
	v_mfma_scale_f32_32x32x64_f8f6f4 v[34:49], v[210:217], v[146:153], v[34:49], v209, v209 op_sel_hi:[0,0,0] blgp:1
	v_exp_f32_e32 v126, v126
	v_exp_f32_e32 v127, v127
	v_exp_f32_e32 v128, v128
	v_exp_f32_e32 v129, v129
	v_exp_f32_e32 v98, v98
	v_exp_f32_e32 v99, v99
	v_exp_f32_e32 v100, v100
	s_add_i32 s61, s61, 1
	s_add_i32 s2, s62, 1
	s_cmp_lg_u32 s62, 2
	s_cselect_b32 s62, s2, 0
	s_mul_i32 s64, s62, 0x6000
	s_add_i32 s2, s64, 0x6000
	s_cmp_eq_u32 s62, 2
	s_cselect_b64 s[8:9], -1, 0
	s_waitcnt vmcnt(0)
	s_and_b64 s[20:21], s[8:9], exec
	s_waitcnt lgkmcnt(0)
	s_barrier
	s_add_i32 s2, s29, s61
	s_add_i32 s2, s2, -1
	s_and_b32 s63, s2, 3
	s_cmp_gt_i32 s33, 63
	s_cselect_b64 s[8:9], -1, 0
	s_cmp_eq_u32 s63, 3
	s_cselect_b64 s[20:21], -1, 0
	s_or_b64 s[8:9], s[8:9], s[20:21]
	s_and_b64 vcc, exec, s[8:9]
	s_cbranch_vccnz .LBB0_812
	s_add_i32 s20, s33, s12
	s_cmpk_lt_i32 s36, 0x100
	s_cselect_b64 s[50:51], -1, 0
	s_lshl_b32 s58, s36, 6
	s_cmpk_gt_i32 s36, 0xff
	s_mov_b64 s[56:57], -1
	s_cbranch_scc1 .LBB0_816
	s_ashr_i32 s21, s20, 31
	s_lshl_b64 s[52:53], s[20:21], 21
	s_add_u32 s8, s44, s52
	s_addc_u32 s9, s45, s53
	s_add_u32 s52, s46, s52
	s_addc_u32 s53, s47, s53
	s_lshl_b64 s[54:55], s[20:21], 20
	s_add_u32 s54, s13, s54
	s_addc_u32 s55, s16, s55
	s_and_b32 s30, s58, 0x3c0
	s_ashr_i32 s64, s36, 4
	s_mov_b64 s[56:57], 0

; DEV unsigned pk_fp8x4(float a, float b, float c, float d) { int w = __builtin_amdgcn_cvt_pk_fp8_f32(a, b, 0, false); w = __builtin_amdgcn_cvt_pk_fp8_f32(c, d, w, true); return (unsigned)w; }
; DEV void sj_advance(SideJob& sj) { sj.j += (int)gridDim.x; while (sj.j >= 384) { sj.j -= 384; ++sj.le; } }
; DEV void sj_tick(const Params& p, int layer, SideJob& sj, LAS char* lds, int tid) {
;     ...
;     } else {
;         const int nl = tid >> 3, kc = tid & 7, blk = nl >> 5, rho = nl & 31; int cl;
;         if (d.mode == 0) cl = 32 * blk + perm32(rho);
;         else if (d.mode >= 2) cl = nl;
;         else { const int i = (rho & 3) + 4 * (rho >> 3), hh = (rho >> 2) & 1; cl = (i < 8 ? 0 : 32) + 16 * blk + 8 * hh + (i & 7); }
;         float v[8];
; #pragma unroll
;         for (int j = 0; j < 8; ++j) v[j] = tile[(8 * kc + j) * 65 + cl];
;         *(u32x2*)(d.dst + (size_t)(d.nt * 64 + nl) * d.ld_dst + d.k0 + 8 * kc) = (u32x2){pk_fp8x4(v[0] * 32.f, v[1] * 32.f, v[2] * 32.f, v[3] * 32.f), pk_fp8x4(v[4] * 32.f, v[5] * 32.f, v[6] * 32.f, v[7] * 32.f)};
;         sj_advance(sj);
.LBB0_819:
	s_cmp_lg_u32 s63, 1
	s_cbranch_scc0 .LBB0_822
	v_add_u32_e32 v168, v196, v197
	ds_read2_b32 v[164:165], v168 offset1:65
	ds_read2_b32 v[166:167], v168 offset0:130 offset1:195
	v_add_u32_e32 v170, 0x400, v168
	ds_read2_b32 v[168:169], v170 offset0:4 offset1:69
	ds_read2_b32 v[170:171], v170 offset0:134 offset1:199
	s_add_i32 s21, s36, s94
	s_waitcnt lgkmcnt(3)
	v_mul_f32_e32 v178, 0x42000000, v164
	v_mul_f32_e32 v165, 0x42000000, v165
	v_mov_b32_e32 v164, 0
	v_cvt_pk_fp8_f32 v164, v178, v165
	s_waitcnt lgkmcnt(1)
	v_mul_f32_e32 v168, 0x42000000, v168
	v_mul_f32_e32 v169, 0x42000000, v169
	v_mov_b32_e32 v165, 0
	v_cvt_pk_fp8_f32 v165, v168, v169
	v_mul_f32_e32 v166, 0x42000000, v166
	v_mul_f32_e32 v167, 0x42000000, v167
	v_cvt_pk_fp8_f32 v164, v166, v167 op_sel:[0,0,1]
	s_waitcnt lgkmcnt(0)
	v_mul_f32_e32 v166, 0x42000000, v170
	v_mul_f32_e32 v167, 0x42000000, v171
	v_cvt_pk_fp8_f32 v165, v166, v167 op_sel:[0,0,1]
	v_lshl_add_u32 v168, s64, 6, v195
	v_mov_b64_e32 v[166:167], s[54:55]
	v_mad_i64_i32 v[166:167], s[54:55], s56, v168, v[166:167]
	v_lshl_add_u64 v[166:167], v[166:167], 0, s[30:31]
	v_lshl_add_u64 v[166:167], v[166:167], 0, v[192:193]
	s_cmpk_lt_i32 s21, 0x180
	global_store_dwordx2 v[166:167], v[164:165], off
	s_cbranch_scc1 .LBB0_834
	v_sub_u32_e64 v164, s21, v251 clamp
	s_mov_b64 s[58:59], 0
	v_readfirstlane_b32 s2, v164
	s_addk_i32 s2, 0x17f
	s_mul_hi_u32 s2, s2, 0xaaaaaaab
	s_lshr_b32 s2, s2, 8
	s_mul_i32 s3, s2, 0xfffffe80
	s_add_i32 s3, s21, s3
	s_add_i32 s2, s33, s2
	s_add_i32 s21, s3, 0xfffffe80
	s_add_i32 s57, s2, 1

; #define LAS __attribute__((address_space(3)))
; DEV void sj_tick(const Params& p, int layer, SideJob& sj, LAS char* lds, int tid) {
;     ...
;     } else if (ph == 1) {
;         const int krow = tid >> 4, c4 = (tid & 15) * 4;
;         LAS float* t0 = tile + krow * 65 + c4; LAS float* t1 = t0 + 32 * 65;
;         t0[0] = sj.v0[0]; t0[1] = sj.v0[1]; t0[2] = sj.v0[2]; t0[3] = sj.v0[3]; t1[0] = sj.v1[0]; t1[1] = sj.v1[1]; t1[2] = sj.v1[2]; t1[3] = sj.v1[3];
.LBB0_823:
	v_add_u32_e32 v164, 0x2080, v194
	s_waitcnt vmcnt(1)
	ds_write2_b32 v194, v182, v183 offset1:1
	ds_write2_b32 v194, v184, v185 offset0:2 offset1:3
	s_waitcnt vmcnt(0)
	ds_write2_b32 v164, v186, v187 offset1:1
	v_add_u32_e32 v164, 0x2088, v194
	s_mov_b32 s21, s36
	s_mov_b32 s57, s33
	ds_write2_b32 v164, v188, v189 offset1:1

; DEV SjDesc sj_desc(const Params& p, int layer, int le_, int j) {
;     SjDesc d; const int le = layer * 64 + le_;
;     if (j < 256) { d.s0 = p.moe_w1 + (size_t)le * 1024 * 512; d.s1 = p.moe_w3 + (size_t)le * 1024 * 512; d.dst = p.ws + WS_W13 + (size_t)le * 1024 * 1024; d.ld = 512; d.ld_dst = 1024; d.k0 = (j & 15) * 64; d.nt = j >> 4; d.mode = 3; }
;     else { const int jj = j - 256; d.s0 = p.moe_w2 + (size_t)le * 512 * 1024; d.s1 = d.s0; d.dst = p.ws + WS_W2 + (size_t)le * 1024 * 512; d.ld = 1024; d.ld_dst = 512; d.k0 = (jj & 7) * 64; d.nt = jj >> 3; d.mode = 2; }
;     return d;
; DEV void sj_tick(const Params& p, int layer, SideJob& sj, LAS char* lds, int tid) {
;     ...
;     if (ph == 0) {
;         const int krow = tid >> 4, c4 = (tid & 15) * 4;
;         const float* a0 = (d.mode == 0 || d.mode == 2) ? d.s0 + (size_t)(d.k0 + krow) * d.ld + d.nt * 64 + c4
;                                         : ((c4 < 32) ? d.s0 + (size_t)(d.k0 + krow) * 512 + d.nt * 32 + c4 : d.s1 + (size_t)(d.k0 + krow) * 512 + d.nt * 32 + c4 - 32);
;         sj.v0 = *(const f32x4*)a0; sj.v1 = *(const f32x4*)(a0 + (size_t)32 * d.ld);
.LBB0_825:
	s_andn2_b64 vcc, exec, s[58:59]
	s_cbranch_vccnz .LBB0_811
	v_add_u32_e32 v164, s30, v191
	v_ashrrev_i32_e32 v165, 31, v164
	s_mov_b64 s[54:55], -1
	s_and_b64 vcc, exec, s[50:51]
	s_cbranch_vccz .LBB0_832
	s_lshl_b32 s50, s64, 5
	v_lshlrev_b64 v[168:169], 11, v[164:165]
	s_ashr_i32 s51, s50, 31
	s_and_saveexec_b64 s[54:55], s[40:41]
	s_xor_b64 s[54:55], exec, s[54:55]
	v_lshl_add_u64 v[166:167], s[52:53], 0, v[168:169]
	v_lshl_add_u64 v[166:167], s[50:51], 2, v[166:167]
	v_lshlrev_b32_e32 v178, 2, v190
	s_movk_i32 s2, 0xff80
	v_lshl_add_u64 v[166:167], v[166:167], 0, v[178:179]
	s_mov_b32 s3, -1
	v_lshl_add_u64 v[166:167], v[166:167], 0, s[2:3]
	s_andn2_saveexec_b64 s[52:53], s[54:55]
	v_lshl_add_u64 v[166:167], s[8:9], 0, v[168:169]
	v_lshl_add_u64 v[166:167], s[50:51], 2, v[166:167]
	v_lshlrev_b32_e32 v178, 2, v190
	v_lshl_add_u64 v[166:167], v[166:167], 0, v[178:179]
	s_or_b64 exec, exec, s[52:53]
	s_mov_b64 s[54:55], 0
.LBB0_832:
	s_andn2_b64 vcc, exec, s[54:55]
	s_cbranch_vccnz .LBB0_810
	v_mad_i64_i32 v[164:165], s[50:51], s20, v164, 0
	v_lshl_add_u64 v[164:165], v[164:165], 2, s[8:9]
	s_lshl_b32 s8, s64, 6
	s_ashr_i32 s9, s8, 31
	v_lshl_add_u64 v[164:165], s[8:9], 2, v[164:165]
	v_lshlrev_b32_e32 v178, 2, v190
	v_lshl_add_u64 v[166:167], v[164:165], 0, v[178:179]
	s_branch .LBB0_810
